# v22 with the two steady-state loop heads aligned to 64 bytes
# baseline (speedup 1.0000x reference)
; #define ISSUE_K(t, sl) do { glds16(Kg + (long)(t) * (KSLOT / 2), (unsigned)__builtin_amdgcn_readfirstlane(kdst + (sl) * KSLOT)); \
;         if (k2) glds16(Kg + (long)(t) * (KSLOT / 2) + 4096, (unsigned)__builtin_amdgcn_readfirstlane(kdst + (sl) * KSLOT + 8192)); } while (0)
; #define ISSUE_V(t, sl) glds16(Vg + (long)(t) * 4096, (unsigned)__builtin_amdgcn_readfirstlane(vdst + (sl) * VSLOT))
; template <bool FOX>
; __device__ __forceinline__ void attn_unit(const Args& A, int b, int h, int qb, LAS char* shm, LAS float* dg) {
;     ...
;     for (int t = 1; t < t_end; ++t) {
;         if (t == 1 && 4 < nti) ISSUE_K(t0 + 4, 0);
;         if (t + 4 < nti) ISSUE_K(t0 + t + 4, t % NS);
;         if (t + 2 < nti) ISSUE_V(t0 + t + 2, (t + 2) % NS);
.Lmla_after_bar:
	s_add_u32 s42, s42, 0x2000
	s_addc_u32 s43, s43, 0
	s_cmp_eq_u32 s27, s96
	v_lshl_add_u64 v[234:235], v[234:235], 0, s[62:63]
	s_cbranch_scc1 .LBB0_867
	s_mov_b32 s26, s27
	s_branch .LBB0_825
	.p2alignl 6, 3212836864

; #define ISSUE_K(t, sl) do { glds16(Kg + (long)(t) * (KSLOT / 2), (unsigned)__builtin_amdgcn_readfirstlane(kdst + (sl) * KSLOT)); \
;         if (k2) glds16(Kg + (long)(t) * (KSLOT / 2) + 4096, (unsigned)__builtin_amdgcn_readfirstlane(kdst + (sl) * KSLOT + 8192)); } while (0)
; #define ISSUE_V(t, sl) glds16(Vg + (long)(t) * 4096, (unsigned)__builtin_amdgcn_readfirstlane(vdst + (sl) * VSLOT))
; template <bool FOX>
; __device__ __forceinline__ void attn_unit(const Args& A, int b, int h, int qb, LAS char* shm, LAS float* dg) {
;     ...
;     for (int t = 1; t < t_end; ++t) {
;         if (t == 1 && 4 < nti) ISSUE_K(t0 + 4, 0);
;         if (t + 4 < nti) ISSUE_K(t0 + t + 4, t % NS);
;         if (t + 2 < nti) ISSUE_V(t0 + t + 2, (t + 2) % NS);
.Lmla_ss1_xdone:
	s_waitcnt vmcnt(4)
	s_barrier
	s_branch .Lmla_ss_done
	.p2alignl 6, 3212836864
